# grid barrier: XCD leaders poll the arrival counter directly instead of a separate generation word (one fewer atomic hop), on top of v43
# baseline (speedup 1.0000x reference)
.LBB0_414:
	s_or_b64 exec, exec, s[4:5]
	s_waitcnt vmcnt(0)
	v_readfirstlane_b32 s2, v3
	v_sub_u32_e32 v4, 0, v2
	s_mov_b64 s[4:5], 0
	v_add_u32_e32 v3, s2, v1
	v_cvt_f32_u32_e32 v1, v2
	v_readlane_b32 s2, v251, 62
	v_readlane_b32 s3, v251, 63
	v_rcp_iflag_f32_e32 v1, v1
	s_nop 0
	v_mul_f32_e32 v1, 0x4f7ffffe, v1
	v_cvt_u32_f32_e32 v1, v1
	v_mul_lo_u32 v4, v4, v1
	v_mul_hi_u32 v4, v1, v4
	v_add_u32_e32 v1, v1, v4
	v_mul_hi_u32 v1, v3, v1
	v_mul_lo_u32 v4, v1, v2
	v_sub_u32_e32 v4, v3, v4
	v_cmp_ge_u32_e32 vcc, v4, v2
	v_add_u32_e32 v5, 1, v1
	v_add_u32_e32 v3, 1, v3
	v_cndmask_b32_e32 v1, v1, v5, vcc
	v_sub_u32_e32 v5, v4, v2
	v_cndmask_b32_e32 v4, v4, v5, vcc
	v_cmp_ge_u32_e32 vcc, v4, v2
	v_add_u32_e32 v4, 1, v1
	s_nop 0
	v_cndmask_b32_e32 v1, v1, v4, vcc
	v_mul_lo_u32 v4, v2, v1
	v_add_u32_e32 v2, v4, v2
	v_cmp_ne_u32_e32 vcc, v3, v2
	v_add_u32_e32 v1, -1, v2
	v_mov_b64_e32 v[2:3], s[2:3]
	s_and_saveexec_b64 s[2:3], vcc
	s_cbranch_execz .LBB0_426
	v_readlane_b32 s4, v251, 60
	v_readlane_b32 s5, v251, 61
	s_mov_b64 s[6:7], 0
	s_nop 3
	global_load_dword v2, v101, s[4:5] sc1
	s_waitcnt vmcnt(0)
	v_cmp_le_u32_e32 vcc, v2, v1
	s_and_saveexec_b64 s[4:5], vcc
	s_cbranch_execz .LBB0_425
	s_mov_b32 s18, 1
	s_branch .LBB0_418

.LBB0_420:
	v_readlane_b32 s10, v251, 60
	v_readlane_b32 s11, v251, 61
	s_add_i32 s18, s18, 1
	s_mov_b64 s[12:13], -1
	s_nop 2
	global_load_dword v2, v101, s[10:11] sc1
	s_waitcnt vmcnt(0)
	v_cmp_gt_u32_e32 vcc, v2, v1
	s_orn2_b64 s[10:11], vcc, exec
	s_branch .LBB0_417

.LBB0_872:
	s_or_b64 exec, exec, s[4:5]
	s_waitcnt vmcnt(0)
	v_readfirstlane_b32 s2, v3
	v_sub_u32_e32 v4, 0, v2
	s_mov_b64 s[4:5], 0
	v_add_u32_e32 v3, s2, v1
	v_cvt_f32_u32_e32 v1, v2
	v_readlane_b32 s2, v251, 62
	v_readlane_b32 s3, v251, 63
	v_rcp_iflag_f32_e32 v1, v1
	s_nop 0
	v_mul_f32_e32 v1, 0x4f7ffffe, v1
	v_cvt_u32_f32_e32 v1, v1
	v_mul_lo_u32 v4, v4, v1
	v_mul_hi_u32 v4, v1, v4
	v_add_u32_e32 v1, v1, v4
	v_mul_hi_u32 v1, v3, v1
	v_mul_lo_u32 v4, v1, v2
	v_sub_u32_e32 v4, v3, v4
	v_cmp_ge_u32_e32 vcc, v4, v2
	v_add_u32_e32 v5, 1, v1
	v_add_u32_e32 v3, 1, v3
	v_cndmask_b32_e32 v1, v1, v5, vcc
	v_sub_u32_e32 v5, v4, v2
	v_cndmask_b32_e32 v4, v4, v5, vcc
	v_cmp_ge_u32_e32 vcc, v4, v2
	v_add_u32_e32 v4, 1, v1
	s_nop 0
	v_cndmask_b32_e32 v1, v1, v4, vcc
	v_mul_lo_u32 v4, v2, v1
	v_add_u32_e32 v2, v4, v2
	v_cmp_ne_u32_e32 vcc, v3, v2
	v_add_u32_e32 v1, -1, v2
	v_mov_b64_e32 v[2:3], s[2:3]
	s_and_saveexec_b64 s[2:3], vcc
	s_cbranch_execz .LBB0_884
	v_readlane_b32 s4, v251, 60
	v_readlane_b32 s5, v251, 61
	s_mov_b64 s[6:7], 0
	s_nop 3
	global_load_dword v2, v101, s[4:5] sc1
	s_waitcnt vmcnt(0)
	v_cmp_le_u32_e32 vcc, v2, v1
	s_and_saveexec_b64 s[4:5], vcc
	s_cbranch_execz .LBB0_883
	s_mov_b32 s16, 1
	s_branch .LBB0_876

.LBB0_878:
	v_readlane_b32 s10, v251, 60
	v_readlane_b32 s11, v251, 61
	s_add_i32 s16, s16, 1
	s_mov_b64 s[12:13], -1
	s_nop 2
	global_load_dword v2, v101, s[10:11] sc1
	s_waitcnt vmcnt(0)
	v_cmp_gt_u32_e32 vcc, v2, v1
	s_orn2_b64 s[10:11], vcc, exec
	s_branch .LBB0_875
